# v19 + P2 streamer store-address VALU moved into MMA2 nop slots (load segment tail keeps only the four stores)
# baseline (speedup 1.0000x reference)
.LBB0_347:
	v_mov_b32_e32 v152, v204
	v_mov_b32_e32 v153, v234
	v_mov_b32_e32 v154, v235
	v_mov_b32_e32 v155, v236
	ds_read_b128 v[158:161], v217
	ds_read_b128 v[162:165], v218
	ds_read_b128 v[166:169], v219
	ds_read_b128 v[170:173], v220
	ds_read_b128 v[148:151], v221
	ds_read_b128 v[144:147], v222
	ds_read_b128 v[140:143], v223
	ds_read_b128 v[136:139], v224
	ds_read_b128 v[174:177], v233
	ds_read_b128 v[178:181], v233 offset:1024
	ds_read_b128 v[182:185], v233 offset:2048
	ds_read_b128 v[186:189], v233 offset:3072
	ds_read_b128 v[190:193], v233 offset:4096
	ds_read_b128 v[194:197], v233 offset:5120
	ds_read_b128 v[234:237], v233 offset:6144
	ds_read_b128 v[238:241], v233 offset:7168
	s_add_i32 s4, s60, s61
	s_mov_b32 s46, s94
	s_add_i32 s94, s94, 1
	s_add_i32 s5, s4, 0x200
	s_add_i32 s16, s33, s61
	s_cmpk_eq_i32 s61, 0x1e00
	s_cselect_b32 s47, s90, s5
	s_cselect_b32 s97, s91, s16
	s_add_i32 s96, s47, 0x80
	s_mov_b32 m0, s82
	s_add_i32 s5, s4, 0x100180
	buffer_load_dwordx4 v214, s[8:11], s5 offen lds
	s_add_i32 s4, s4, 0x180180
	s_mov_b32 m0, s85
	s_add_i32 vcc_lo, s97, 0x80
	buffer_load_dwordx4 v214, s[8:11], s4 offen lds
	s_lshr_b32 s4, s94, 2
	s_mul_i32 s5, s4, s34
	s_add_i32 s16, s5, s2
	s_cmp_lt_i32 s4, s3
	s_cselect_b64 s[4:5], -1, 0
	s_and_b64 s[44:45], s[4:5], exec
	s_cselect_b32 s16, s16, 0
	s_bfe_u32 s17, s94, 0x10001
	s_or_b32 s17, s17, s83
	s_bfe_u32 s67, s16, 0x50007
	s_bfe_u32 s36, s16, 0x50002
	s_and_b32 s95, s16, 3
	s_cmpk_gt_i32 s16, 0xfff
	s_cselect_b64 s[44:45], -1, 0
	v_lshl_or_b32 v156, s17, 3, v216
	s_and_b64 s[16:17], s[44:45], exec
	s_cselect_b32 s16, s25, s21
	s_cselect_b32 s17, s24, s20
	s_lshl_b32 vcc_hi, s67, 23
	s_add_u32 s17, s17, vcc_hi
	s_addc_u32 s16, s16, 0
	s_lshl_b32 vcc_hi, s36, 18
	s_add_u32 s17, s17, vcc_hi
	s_addc_u32 vcc_hi, s16, 0
	s_lshl_b32 s16, s95, 9
	s_add_u32 s16, s17, s16
	v_and_or_b32 v204, s66, 2, v200
	s_addc_u32 s17, vcc_hi, 0
	v_lshlrev_b64 v[128:129], 11, v[204:205]
	v_lshl_add_u64 v[128:129], s[16:17], 0, v[128:129]
	v_lshlrev_b32_e32 v204, 4, v156
	v_lshl_add_u64 v[132:133], v[128:129], 0, v[204:205]
	global_load_dwordx4 v[128:131], v[132:133], off nt
	s_nop 0
	global_load_dwordx4 v[132:135], v[132:133], off offset:2048 nt
	s_waitcnt vmcnt(10)
	s_waitcnt lgkmcnt(8)
	s_barrier
	s_setprio 1
	s_waitcnt lgkmcnt(7)
	v_mfma_f32_16x16x32_bf16 v[124:127], v[158:161], v[174:177], v[124:127]
	s_waitcnt lgkmcnt(6)
	v_mfma_f32_16x16x32_bf16 v[124:127], v[162:165], v[178:181], v[124:127]
	v_mfma_f32_16x16x32_bf16 v[120:123], v[166:169], v[174:177], v[120:123]
	s_nop 0
	v_mfma_f32_16x16x32_bf16 v[120:123], v[170:173], v[178:181], v[120:123]
	s_waitcnt lgkmcnt(5)
	v_mfma_f32_16x16x32_bf16 v[116:119], v[158:161], v[182:185], v[116:119]
	s_waitcnt lgkmcnt(4)
	v_mfma_f32_16x16x32_bf16 v[116:119], v[162:165], v[186:189], v[116:119]
	v_mfma_f32_16x16x32_bf16 v[112:115], v[166:169], v[182:185], v[112:115]
	s_nop 0
	v_mfma_f32_16x16x32_bf16 v[112:115], v[170:173], v[186:189], v[112:115]
	s_waitcnt lgkmcnt(3)
	v_mfma_f32_16x16x32_bf16 v[108:111], v[158:161], v[190:193], v[108:111]
	s_waitcnt lgkmcnt(2)
	v_mfma_f32_16x16x32_bf16 v[108:111], v[162:165], v[194:197], v[108:111]
	v_mfma_f32_16x16x32_bf16 v[104:107], v[166:169], v[190:193], v[104:107]
	s_nop 0
	v_mfma_f32_16x16x32_bf16 v[104:107], v[170:173], v[194:197], v[104:107]
	s_waitcnt lgkmcnt(1)
	v_mfma_f32_16x16x32_bf16 v[100:103], v[158:161], v[234:237], v[100:103]
	s_waitcnt lgkmcnt(0)
	v_mfma_f32_16x16x32_bf16 v[100:103], v[162:165], v[238:241], v[100:103]
	v_mfma_f32_16x16x32_bf16 v[96:99], v[166:169], v[234:237], v[96:99]
	s_nop 0
	v_mfma_f32_16x16x32_bf16 v[96:99], v[170:173], v[238:241], v[96:99]
	s_setprio 0
	s_setprio 1
	v_mfma_f32_16x16x32_bf16 v[92:95], v[148:151], v[174:177], v[92:95]
	s_nop 0
	v_mfma_f32_16x16x32_bf16 v[92:95], v[144:147], v[178:181], v[92:95]
	v_mfma_f32_16x16x32_bf16 v[88:91], v[140:143], v[174:177], v[88:91]
	s_nop 0
	v_mfma_f32_16x16x32_bf16 v[88:91], v[136:139], v[178:181], v[88:91]
	v_mfma_f32_16x16x32_bf16 v[84:87], v[148:151], v[182:185], v[84:87]
	s_nop 0
	v_mfma_f32_16x16x32_bf16 v[84:87], v[144:147], v[186:189], v[84:87]
	v_mfma_f32_16x16x32_bf16 v[80:83], v[140:143], v[182:185], v[80:83]
	s_nop 0
	v_mfma_f32_16x16x32_bf16 v[80:83], v[136:139], v[186:189], v[80:83]
	v_mfma_f32_16x16x32_bf16 v[76:79], v[148:151], v[190:193], v[76:79]
	s_nop 0
	v_mfma_f32_16x16x32_bf16 v[76:79], v[144:147], v[194:197], v[76:79]
	v_mfma_f32_16x16x32_bf16 v[72:75], v[140:143], v[190:193], v[72:75]
	s_nop 0
	v_mfma_f32_16x16x32_bf16 v[72:75], v[136:139], v[194:197], v[72:75]
	v_mfma_f32_16x16x32_bf16 v[68:71], v[148:151], v[234:237], v[68:71]
	s_nop 0
	v_mfma_f32_16x16x32_bf16 v[68:71], v[144:147], v[238:241], v[68:71]
	v_mfma_f32_16x16x32_bf16 v[64:67], v[140:143], v[234:237], v[64:67]
	s_nop 0
	v_mfma_f32_16x16x32_bf16 v[64:67], v[136:139], v[238:241], v[64:67]
	s_setprio 0
	s_barrier
	ds_read_b128 v[174:177], v233 offset:16384
	ds_read_b128 v[178:181], v233 offset:17408
	ds_read_b128 v[182:185], v233 offset:18432
	ds_read_b128 v[186:189], v233 offset:19456
	ds_read_b128 v[190:193], v233 offset:20480
	ds_read_b128 v[194:197], v233 offset:21504
	ds_read_b128 v[234:237], v233 offset:22528
	ds_read_b128 v[238:241], v233 offset:23552
	s_mov_b32 m0, s65
	s_add_i32 s16, s97, 0x100000
	buffer_load_dwordx4 v215, s[12:15], s97 offen lds
	s_mov_b32 m0, s68
	s_nop 0
	buffer_load_dwordx4 v215, s[12:15], s16 offen lds
	s_add_i32 s16, s97, 0x10000
	s_mov_b32 m0, s69
	s_nop 0
	buffer_load_dwordx4 v215, s[12:15], s16 offen lds
	s_add_i32 s16, s97, 0x110000
	s_mov_b32 m0, s70
	s_nop 0
	buffer_load_dwordx4 v215, s[12:15], s16 offen lds
	s_mov_b32 m0, s64
	s_add_i32 s16, s47, 0x80000
	buffer_load_dwordx4 v214, s[8:11], s47 offen lds
	s_mov_b32 m0, s71
	s_nop 0
	buffer_load_dwordx4 v214, s[8:11], s16 offen lds
	s_lshl_b32 s99, s67, 10
	s_lshl_b32 s100, s95, 8
	s_or_b32 s99, s99, s100
	s_cmp_lg_u64 s[44:45], 0
	s_cselect_b32 s100, 8, 0
	s_or_b32 s99, s99, s100
	s_lshl_b32 s36, s36, 7
	s_mov_b32 s100, 0x1000
	s_mov_b32 s101, 0
	s_waitcnt vmcnt(10)
	s_waitcnt lgkmcnt(6)
	s_barrier
	s_setprio 1
	s_waitcnt lgkmcnt(7)
	v_mfma_f32_16x16x32_bf16 v[60:63], v[158:161], v[174:177], v[60:63]
	s_waitcnt lgkmcnt(6)
	v_mfma_f32_16x16x32_bf16 v[60:63], v[162:165], v[178:181], v[60:63]
	v_mfma_f32_16x16x32_bf16 v[56:59], v[166:169], v[174:177], v[56:59]
	v_lshlrev_b32_e32 v242, 3, v156
	v_mfma_f32_16x16x32_bf16 v[56:59], v[170:173], v[178:181], v[56:59]
	s_waitcnt lgkmcnt(5)
	v_mfma_f32_16x16x32_bf16 v[52:55], v[158:161], v[182:185], v[52:55]
	s_waitcnt lgkmcnt(4)
	v_mfma_f32_16x16x32_bf16 v[52:55], v[162:165], v[186:189], v[52:55]
	v_mfma_f32_16x16x32_bf16 v[48:51], v[166:169], v[182:185], v[48:51]
	v_and_b32_e32 v242, 0xf0, v242
	v_mfma_f32_16x16x32_bf16 v[48:51], v[170:173], v[186:189], v[48:51]
	s_waitcnt lgkmcnt(3)
	v_mfma_f32_16x16x32_bf16 v[44:47], v[158:161], v[190:193], v[44:47]
	s_waitcnt lgkmcnt(2)
	v_mfma_f32_16x16x32_bf16 v[44:47], v[162:165], v[194:197], v[44:47]
	v_mfma_f32_16x16x32_bf16 v[40:43], v[166:169], v[190:193], v[40:43]
	v_or_b32_e32 v242, s99, v242
	v_mfma_f32_16x16x32_bf16 v[40:43], v[170:173], v[194:197], v[40:43]
	s_waitcnt lgkmcnt(1)
	v_mfma_f32_16x16x32_bf16 v[36:39], v[158:161], v[234:237], v[36:39]
	s_waitcnt lgkmcnt(0)
	v_mfma_f32_16x16x32_bf16 v[36:39], v[162:165], v[238:241], v[36:39]
	v_mfma_f32_16x16x32_bf16 v[32:35], v[166:169], v[234:237], v[32:35]
	v_or_b32_e32 v204, v242, v202
	v_mfma_f32_16x16x32_bf16 v[32:35], v[170:173], v[238:241], v[32:35]
	s_setprio 0
	s_setprio 1
	v_mfma_f32_16x16x32_bf16 v[28:31], v[148:151], v[174:177], v[28:31]
	v_lshlrev_b64 v[242:243], 12, v[204:205]
	v_mfma_f32_16x16x32_bf16 v[28:31], v[144:147], v[178:181], v[28:31]
	v_mfma_f32_16x16x32_bf16 v[24:27], v[140:143], v[174:177], v[24:27]
	v_lshl_add_u64 v[242:243], s[6:7], 0, v[242:243]
	v_mfma_f32_16x16x32_bf16 v[24:27], v[136:139], v[178:181], v[24:27]
	v_mfma_f32_16x16x32_bf16 v[20:23], v[148:151], v[182:185], v[20:23]
	v_lshl_add_u64 v[242:243], v[242:243], 0, s[36:37]
	v_mfma_f32_16x16x32_bf16 v[20:23], v[144:147], v[186:189], v[20:23]
	v_mfma_f32_16x16x32_bf16 v[16:19], v[140:143], v[182:185], v[16:19]
	v_lshl_add_u64 v[242:243], v[242:243], 0, v[200:201]
	v_mfma_f32_16x16x32_bf16 v[16:19], v[136:139], v[186:189], v[16:19]
	v_mfma_f32_16x16x32_bf16 v[12:15], v[148:151], v[190:193], v[12:15]
	v_lshl_add_u64 v[244:245], v[242:243], 0, s[100:101]
	v_mfma_f32_16x16x32_bf16 v[12:15], v[144:147], v[194:197], v[12:15]
	v_mfma_f32_16x16x32_bf16 v[8:11], v[140:143], v[190:193], v[8:11]
	v_lshl_add_u64 v[246:247], v[244:245], 0, s[100:101]
	v_mfma_f32_16x16x32_bf16 v[8:11], v[136:139], v[194:197], v[8:11]
	v_mfma_f32_16x16x32_bf16 v[4:7], v[148:151], v[234:237], v[4:7]
	v_lshl_add_u64 v[254:255], v[246:247], 0, s[100:101]
	v_mfma_f32_16x16x32_bf16 v[4:7], v[144:147], v[238:241], v[4:7]
	v_mfma_f32_16x16x32_bf16 v[0:3], v[140:143], v[234:237], v[0:3]
	s_nop 0
	v_mfma_f32_16x16x32_bf16 v[0:3], v[136:139], v[238:241], v[0:3]
	s_setprio 0
	s_barrier
	ds_read_b128 v[136:139], v225
	ds_read_b128 v[140:143], v226
	ds_read_b128 v[144:147], v227
	ds_read_b128 v[148:151], v228
	ds_read_b128 v[158:161], v229
	ds_read_b128 v[162:165], v230
	ds_read_b128 v[166:169], v231
	ds_read_b128 v[170:173], v232
	ds_read_b128 v[174:177], v233 offset:32768
	ds_read_b128 v[178:181], v233 offset:33792
	ds_read_b128 v[182:185], v233 offset:34816
	ds_read_b128 v[186:189], v233 offset:35840
	ds_read_b128 v[190:193], v233 offset:36864
	ds_read_b128 v[194:197], v233 offset:37888
	ds_read_b128 v[234:237], v233 offset:38912
	ds_read_b128 v[238:241], v233 offset:39936
	s_mov_b32 m0, s72
	s_add_i32 s16, s47, 0x100000
	buffer_load_dwordx4 v214, s[8:11], s16 offen lds
	s_add_i32 s16, s47, 0x180000
	s_mov_b32 m0, s73
	s_nop 0
	buffer_load_dwordx4 v214, s[8:11], s16 offen lds
	s_waitcnt vmcnt(10)
	s_waitcnt lgkmcnt(8)
	s_barrier
	s_setprio 1
	s_waitcnt lgkmcnt(7)
	v_mfma_f32_16x16x32_bf16 v[124:127], v[136:139], v[174:177], v[124:127]
	s_waitcnt lgkmcnt(6)
	v_mfma_f32_16x16x32_bf16 v[124:127], v[140:143], v[178:181], v[124:127]
	v_mfma_f32_16x16x32_bf16 v[120:123], v[144:147], v[174:177], v[120:123]
	s_nop 0
	v_mfma_f32_16x16x32_bf16 v[120:123], v[148:151], v[178:181], v[120:123]
	s_waitcnt lgkmcnt(5)
	v_mfma_f32_16x16x32_bf16 v[116:119], v[136:139], v[182:185], v[116:119]
	s_waitcnt lgkmcnt(4)
	v_mfma_f32_16x16x32_bf16 v[116:119], v[140:143], v[186:189], v[116:119]
	v_mfma_f32_16x16x32_bf16 v[112:115], v[144:147], v[182:185], v[112:115]
	s_nop 0
	v_mfma_f32_16x16x32_bf16 v[112:115], v[148:151], v[186:189], v[112:115]
	s_waitcnt lgkmcnt(3)
	v_mfma_f32_16x16x32_bf16 v[108:111], v[136:139], v[190:193], v[108:111]
	s_waitcnt lgkmcnt(2)
	v_mfma_f32_16x16x32_bf16 v[108:111], v[140:143], v[194:197], v[108:111]
	v_mfma_f32_16x16x32_bf16 v[104:107], v[144:147], v[190:193], v[104:107]
	s_nop 0
	v_mfma_f32_16x16x32_bf16 v[104:107], v[148:151], v[194:197], v[104:107]
	s_waitcnt lgkmcnt(1)
	v_mfma_f32_16x16x32_bf16 v[100:103], v[136:139], v[234:237], v[100:103]
	s_waitcnt lgkmcnt(0)
	v_mfma_f32_16x16x32_bf16 v[100:103], v[140:143], v[238:241], v[100:103]
	v_mfma_f32_16x16x32_bf16 v[96:99], v[144:147], v[234:237], v[96:99]
	s_nop 0
	v_mfma_f32_16x16x32_bf16 v[96:99], v[148:151], v[238:241], v[96:99]
	s_setprio 0
	s_setprio 1
	v_mfma_f32_16x16x32_bf16 v[92:95], v[158:161], v[174:177], v[92:95]
	s_nop 0
	v_mfma_f32_16x16x32_bf16 v[92:95], v[162:165], v[178:181], v[92:95]
	v_mfma_f32_16x16x32_bf16 v[88:91], v[166:169], v[174:177], v[88:91]
	s_nop 0
	v_mfma_f32_16x16x32_bf16 v[88:91], v[170:173], v[178:181], v[88:91]
	v_mfma_f32_16x16x32_bf16 v[84:87], v[158:161], v[182:185], v[84:87]
	s_nop 0
	v_mfma_f32_16x16x32_bf16 v[84:87], v[162:165], v[186:189], v[84:87]
	v_mfma_f32_16x16x32_bf16 v[80:83], v[166:169], v[182:185], v[80:83]
	s_nop 0
	v_mfma_f32_16x16x32_bf16 v[80:83], v[170:173], v[186:189], v[80:83]
	v_mfma_f32_16x16x32_bf16 v[76:79], v[158:161], v[190:193], v[76:79]
	s_nop 0
	v_mfma_f32_16x16x32_bf16 v[76:79], v[162:165], v[194:197], v[76:79]
	v_mfma_f32_16x16x32_bf16 v[72:75], v[166:169], v[190:193], v[72:75]
	s_nop 0
	v_mfma_f32_16x16x32_bf16 v[72:75], v[170:173], v[194:197], v[72:75]
	v_mfma_f32_16x16x32_bf16 v[68:71], v[158:161], v[234:237], v[68:71]
	s_nop 0
	v_mfma_f32_16x16x32_bf16 v[68:71], v[162:165], v[238:241], v[68:71]
	v_mfma_f32_16x16x32_bf16 v[64:67], v[166:169], v[234:237], v[64:67]
	s_nop 0
	v_mfma_f32_16x16x32_bf16 v[64:67], v[170:173], v[238:241], v[64:67]
	s_setprio 0
	s_barrier
	ds_read_b128 v[174:177], v233 offset:49152
	ds_read_b128 v[178:181], v233 offset:50176
	ds_read_b128 v[182:185], v233 offset:51200
	ds_read_b128 v[186:189], v233 offset:52224
	ds_read_b128 v[190:193], v233 offset:53248
	ds_read_b128 v[194:197], v233 offset:54272
	ds_read_b128 v[234:237], v233 offset:55296
	ds_read_b128 v[238:241], v233 offset:56320
	s_mov_b32 m0, s76
	s_add_i32 s16, s97, 0x100080
	buffer_load_dwordx4 v215, s[12:15], vcc_lo offen lds
	s_mov_b32 m0, s77
	s_add_i32 s47, s47, 0x80080
	buffer_load_dwordx4 v215, s[12:15], s16 offen lds
	s_add_i32 s16, s97, 0x10080
	s_mov_b32 m0, s80
	s_add_i32 s97, s97, 0x110080
	buffer_load_dwordx4 v215, s[12:15], s16 offen lds
	s_mov_b32 m0, s81
	s_nop 0
	buffer_load_dwordx4 v215, s[12:15], s97 offen lds
	s_mov_b32 m0, s78
	s_nop 0
	buffer_load_dwordx4 v214, s[8:11], s96 offen lds
	s_mov_b32 m0, s79
	s_nop 0
	buffer_load_dwordx4 v214, s[8:11], s47 offen lds
	s_bitcmp0_b32 s46, 0
	s_mov_b32 s98, 0xffff
	s_cselect_b32 s98, 0xffff0000, s98
	s_waitcnt vmcnt(8)
	s_waitcnt lgkmcnt(6)
	s_barrier
	s_setprio 1
	s_waitcnt lgkmcnt(7)
	v_mfma_f32_16x16x32_bf16 v[60:63], v[136:139], v[174:177], v[60:63]
	s_waitcnt lgkmcnt(6)
	v_mfma_f32_16x16x32_bf16 v[60:63], v[140:143], v[178:181], v[60:63]
	v_mfma_f32_16x16x32_bf16 v[56:59], v[144:147], v[174:177], v[56:59]
	v_mul_f32_e32 v128, 0x42800000, v128
	v_mfma_f32_16x16x32_bf16 v[56:59], v[148:151], v[178:181], v[56:59]
	v_mul_f32_e32 v130, 0x42800000, v130
	s_waitcnt lgkmcnt(5)
	v_mfma_f32_16x16x32_bf16 v[52:55], v[136:139], v[182:185], v[52:55]
	s_waitcnt lgkmcnt(4)
	v_mfma_f32_16x16x32_bf16 v[52:55], v[140:143], v[186:189], v[52:55]
	v_mfma_f32_16x16x32_bf16 v[48:51], v[144:147], v[182:185], v[48:51]
	v_mul_f32_e32 v132, 0x42800000, v132
	v_mfma_f32_16x16x32_bf16 v[48:51], v[148:151], v[186:189], v[48:51]
	v_mul_f32_e32 v134, 0x42800000, v134
	s_waitcnt lgkmcnt(3)
	v_mfma_f32_16x16x32_bf16 v[44:47], v[136:139], v[190:193], v[44:47]
	s_waitcnt lgkmcnt(2)
	v_mfma_f32_16x16x32_bf16 v[44:47], v[140:143], v[194:197], v[44:47]
	v_mfma_f32_16x16x32_bf16 v[40:43], v[144:147], v[190:193], v[40:43]
	v_mul_f32_e32 v129, 0x42800000, v129
	v_mfma_f32_16x16x32_bf16 v[40:43], v[148:151], v[194:197], v[40:43]
	v_mul_f32_e32 v131, 0x42800000, v131
	s_waitcnt lgkmcnt(1)
	v_mfma_f32_16x16x32_bf16 v[36:39], v[136:139], v[234:237], v[36:39]
	s_waitcnt lgkmcnt(0)
	v_mfma_f32_16x16x32_bf16 v[36:39], v[140:143], v[238:241], v[36:39]
	v_mfma_f32_16x16x32_bf16 v[32:35], v[144:147], v[234:237], v[32:35]
	v_mul_f32_e32 v133, 0x42800000, v133
	v_mfma_f32_16x16x32_bf16 v[32:35], v[148:151], v[238:241], v[32:35]
	v_mul_f32_e32 v135, 0x42800000, v135
	s_setprio 0
	s_setprio 1
	v_mfma_f32_16x16x32_bf16 v[28:31], v[158:161], v[174:177], v[28:31]
	v_cvt_pk_fp8_f32 v204, v128, v132
	v_mfma_f32_16x16x32_bf16 v[28:31], v[162:165], v[178:181], v[28:31]
	v_mfma_f32_16x16x32_bf16 v[24:27], v[166:169], v[174:177], v[24:27]
	v_cvt_pk_fp8_f32 v204, v128, v132 op_sel:[0,0,1]
	v_mfma_f32_16x16x32_bf16 v[24:27], v[170:173], v[178:181], v[24:27]
	v_mfma_f32_16x16x32_bf16 v[20:23], v[158:161], v[182:185], v[20:23]
	v_cvt_pk_fp8_f32 v250, v129, v133
	v_mfma_f32_16x16x32_bf16 v[20:23], v[162:165], v[186:189], v[20:23]
	v_mfma_f32_16x16x32_bf16 v[16:19], v[166:169], v[182:185], v[16:19]
	v_cvt_pk_fp8_f32 v250, v129, v133 op_sel:[0,0,1]
	v_mfma_f32_16x16x32_bf16 v[16:19], v[170:173], v[186:189], v[16:19]
	v_mfma_f32_16x16x32_bf16 v[12:15], v[158:161], v[190:193], v[12:15]
	v_cvt_pk_fp8_f32 v251, v130, v134
	v_mfma_f32_16x16x32_bf16 v[12:15], v[162:165], v[194:197], v[12:15]
	v_bfi_b32 v152, s98, v204, v152
	v_mfma_f32_16x16x32_bf16 v[8:11], v[166:169], v[190:193], v[8:11]
	v_cvt_pk_fp8_f32 v251, v130, v134 op_sel:[0,0,1]
	v_mfma_f32_16x16x32_bf16 v[8:11], v[170:173], v[194:197], v[8:11]
	v_bfi_b32 v153, s98, v250, v153
	v_mfma_f32_16x16x32_bf16 v[4:7], v[158:161], v[234:237], v[4:7]
	v_cvt_pk_fp8_f32 v252, v131, v135
	v_mfma_f32_16x16x32_bf16 v[4:7], v[162:165], v[238:241], v[4:7]
	v_bfi_b32 v154, s98, v251, v154
	v_mfma_f32_16x16x32_bf16 v[0:3], v[166:169], v[234:237], v[0:3]
	v_cvt_pk_fp8_f32 v252, v131, v135 op_sel:[0,0,1]
	v_mfma_f32_16x16x32_bf16 v[0:3], v[170:173], v[238:241], v[0:3]
	v_bfi_b32 v155, s98, v252, v155
	s_setprio 0
	s_barrier
	s_bitcmp0_b32 s46, 0
	s_mov_b64 s[46:47], -1
	s_cbranch_scc0 .LBB0_345
	s_andn2_b64 vcc, exec, s[4:5]
	s_cbranch_vccnz .LBB0_345
	global_store_dword v[242:243], v152, off
	global_store_dword v[244:245], v153, off
	global_store_dword v[246:247], v154, off
	global_store_dword v[254:255], v155, off
	s_branch .LBB0_345
